# v54 plus P4 early key-fragment loads: the first key fragments of both selection passes are issued before the preceding Q-wait/barrier/LDS-clear
# speedup vs baseline: 1.0082x; 1.0050x over previous
; #define LAS __attribute__((address_space(3)))
; __device__ __forceinline__ bf16 f2bf(float f) { unsigned u = __float_as_uint(f); return (bf16)((u + 0x7fffu + ((u >> 16) & 1u)) >> 16); }
; #define DSA2_LOADK(dst, kt_) do { _Pragma("unroll") for (int s = 0; s < 4; ++s) dst[s] = *(const bf16x8*)(kp + (size_t)(32 * (kt_)) * Y0P + 16 * s); } while (0)
; template <int STAGE>
; __device__ __forceinline__ void pass2(LAS unsigned char* lds, const bf16* kbase, int g, int t0, const bf16x8 (&qf)[4][4], const f32x4 lo4, const f32x4 hi4, int wave, int r, int h2) {
;     ...
;     int kt = wave;
;     if (kt <= g) DSA2_LOADK(kf, kt);
; __device__ __forceinline__ bool run_unit2(LAS unsigned char* lds, const bf16* y0, const float* aux, unsigned* maskg, int b, int g, int tid_in, int wave, int lane) {
;     ...
;     for (int i = tid; i < (OFF2_TB) / 4; i += NTHR) ((LAS unsigned*)lds)[i] = 0u;
;     if (tid < 32) { ((LAS unsigned*)(lds + OFF2_CNT))[tid] = 0u; }
;     if (tid == 0) ((LAS int*)(lds + OFF2_FLAG))[0] = 0;
;     bf16x8 qf[4][4];
;     {
;         const bf16* qp = y0 + (rowbase + t0 + r) * (size_t)Y0P + Y0_IQ + 8 * h2;
; #pragma unroll
;         for (int hd = 0; hd < 4; ++hd)
; #pragma unroll
;             for (int s = 0; s < 4; ++s) qf[hd][s] = *(const bf16x8*)(qp + hd * 64 + 16 * s);
;     }
;     const f32x4 w4 = *(const f32x4*)(aux + (rowbase + t0 + r) * 16 + 8);
;     f32x4 lo4, hi4;
; #pragma unroll
;     for (int hd = 0; hd < 4; ++hd) {
;         const float wsc = w4[hd] * 0.0625f;
;         lo4[hd] = (w4[hd] >= 0.f) ? 0.f : -INFINITY; hi4[hd] = (w4[hd] >= 0.f) ? INFINITY : 0.f;
; #pragma unroll
;         for (int s = 0; s < 4; ++s) {
;             bf16x8 a = qf[hd][s];
; #pragma unroll
;             for (int j = 0; j < 8; ++j) a[j] = (short)f2bf(__uint_as_float(((unsigned)(unsigned short)a[j]) << 16) * wsc);
;             qf[hd][s] = a;
;         }
;     }
;     const bf16* kbase = y0 + rowbase * (size_t)Y0P + Y0_IK;
;     __syncthreads();
.LBB0_779:
	s_or_b64 exec, exec, s[2:3]
	v_cmp_gt_i32_e32 vcc, 32, v206
	s_and_saveexec_b64 s[2:3], vcc
	v_lshl_add_u32 v0, v206, 2, 0
	v_add_u32_e32 v0, 0x18200, v0
	ds_write_b32 v0, v177
	s_or_b64 exec, exec, s[2:3]
	v_cmp_eq_u32_e32 vcc, 0, v206
	s_and_saveexec_b64 s[2:3], vcc
	v_mov_b32_e32 v0, s88
	ds_write_b32 v0, v177
	s_or_b64 exec, exec, s[2:3]
	s_andn2_b32 s64, 0xff, s0
	s_lshr_b32 s66, s0, 8
	v_and_b32_e32 v218, 31, v217
	s_lshl_b32 s41, s64, 5
	v_ashrrev_i32_e32 v219, 5, v217
	s_lshl_b64 s[76:77], s[66:67], 13
	v_or_b32_e32 v211, s41, v218
	v_or_b32_e32 v0, s76, v211
	v_mov_b64_e32 v[2:3], s[44:45]
	s_waitcnt vmcnt(0)
	v_lshlrev_b32_e32 v48, 3, v219
	v_mov_b32_e32 v1, s77
	v_mad_u64_u32 v[2:3], s[0:1], v0, s33, v[2:3]
	v_ashrrev_i32_e32 v49, 31, v48
	v_mad_u32_u24 v3, s77, v187, v3
	v_lshlrev_b64 v[50:51], 1, v[48:49]
	v_lshlrev_b64 v[0:1], 6, v[0:1]
	v_lshl_add_u64 v[2:3], v[2:3], 0, v[50:51]
	v_lshl_add_u64 v[0:1], s[46:47], 0, v[0:1]
	global_load_dwordx4 v[16:19], v[0:1], off offset:32
	v_add_co_u32_e32 v0, vcc, s31, v2
	s_mul_i32 s78, s66, 0x3800000
	s_nop 0
	v_addc_co_u32_e32 v1, vcc, 0, v3, vcc
	global_load_dwordx4 v[52:55], v[0:1], off offset:2048
	v_lshl_add_u64 v[0:1], v[2:3], 0, s[28:29]
	global_load_dwordx4 v[56:59], v[0:1], off offset:32
	global_load_dwordx4 v[60:63], v[0:1], off offset:64
	global_load_dwordx4 v[76:79], v[0:1], off offset:96
	global_load_dwordx4 v[80:83], v[0:1], off offset:128
	global_load_dwordx4 v[44:47], v[0:1], off offset:160
	global_load_dwordx4 v[40:43], v[0:1], off offset:192
	global_load_dwordx4 v[36:39], v[0:1], off offset:224
	global_load_dwordx4 v[32:35], v[0:1], off offset:256
	global_load_dwordx4 v[28:31], v[0:1], off offset:288
	global_load_dwordx4 v[24:27], v[0:1], off offset:320
	global_load_dwordx4 v[20:23], v[0:1], off offset:352
	global_load_dwordx4 v[12:15], v[0:1], off offset:384
	global_load_dwordx4 v[8:11], v[0:1], off offset:416
	global_load_dwordx4 v[4:7], v[0:1], off offset:448
	s_nop 0
	global_load_dwordx4 v[0:3], v[0:1], off offset:480
	s_mul_hi_u32 s79, s66, 0x3800000
	s_add_u32 s0, s44, s78
	s_addc_u32 s1, s45, s79
	s_add_u32 s80, s0, 0x1a00
	s_addc_u32 s81, s1, 0
	v_mul_u32_u24_e32 v176, 0x1c00, v218
	v_readlane_b32 s0, v254, 24
	s_cmp_le_u32 s0, s64
	s_cselect_b64 s[82:83], -1, 0
	s_cmp_gt_u32 s0, s64
	v_lshl_add_u64 v[180:181], s[80:81], 0, v[176:177]
	v_lshl_add_u64 v[180:181], v[180:181], 0, v[50:51]
	v_lshl_add_u64 v[180:181], v[180:181], 0, s[36:37]
	global_load_dwordx4 v[140:143], v[180:181], off
	global_load_dwordx4 v[136:139], v[180:181], off offset:32
	global_load_dwordx4 v[132:135], v[180:181], off offset:64
	global_load_dwordx4 v[128:131], v[180:181], off offset:96
	s_waitcnt lgkmcnt(0)
	s_barrier
	s_waitcnt vmcnt(4)
	v_and_b32_e32 v71, 0xffff0000, v57
	v_lshlrev_b32_e32 v70, 16, v57
	v_and_b32_e32 v57, 0xffff0000, v58
	v_and_b32_e32 v73, 0xffff0000, v59
	v_lshlrev_b32_e32 v72, 16, v59
	v_mul_f32_e32 v84, 0x3d800000, v16
	v_cmp_le_f32_e32 vcc, 0, v16
	v_and_b32_e32 v65, 0xffff0000, v52
	v_lshlrev_b32_e32 v64, 16, v52
	v_and_b32_e32 v67, 0xffff0000, v53
	v_lshlrev_b32_e32 v66, 16, v53
	v_and_b32_e32 v53, 0xffff0000, v54
	v_lshlrev_b32_e32 v52, 16, v54
	v_and_b32_e32 v69, 0xffff0000, v55
	v_lshlrev_b32_e32 v68, 16, v55
	v_and_b32_e32 v55, 0xffff0000, v56
	v_lshlrev_b32_e32 v54, 16, v56
	v_lshlrev_b32_e32 v56, 16, v58
	v_pk_mul_f32 v[58:59], v[84:85], v[64:65] op_sel_hi:[0,1]
	v_pk_mul_f32 v[64:65], v[84:85], v[66:67] op_sel_hi:[0,1]
	v_pk_mul_f32 v[52:53], v[84:85], v[52:53] op_sel_hi:[0,1]
	v_pk_mul_f32 v[66:67], v[84:85], v[68:69] op_sel_hi:[0,1]
	v_pk_mul_f32 v[54:55], v[84:85], v[54:55] op_sel_hi:[0,1]
	v_pk_mul_f32 v[68:69], v[84:85], v[70:71] op_sel_hi:[0,1]
	v_pk_mul_f32 v[56:57], v[84:85], v[56:57] op_sel_hi:[0,1]
	v_pk_mul_f32 v[70:71], v[84:85], v[72:73] op_sel_hi:[0,1]
	v_bfe_u32 v16, v67, 16, 1
	v_bfe_u32 v72, v66, 16, 1
	v_bfe_u32 v73, v53, 16, 1
	v_bfe_u32 v74, v52, 16, 1
	v_bfe_u32 v75, v65, 16, 1
	v_bfe_u32 v85, v64, 16, 1
	v_bfe_u32 v86, v59, 16, 1
	v_bfe_u32 v87, v58, 16, 1
	v_add3_u32 v58, v58, v87, s73
	v_add3_u32 v59, v59, v86, s73
	v_add3_u32 v64, v64, v85, s73
	v_add3_u32 v65, v65, v75, s73
	v_add3_u32 v52, v52, v74, s73
	v_add3_u32 v53, v53, v73, s73
	v_add3_u32 v66, v66, v72, s73
	v_add3_u32 v16, v67, v16, s73
	v_bfe_u32 v88, v71, 16, 1
	v_bfe_u32 v89, v70, 16, 1
	v_bfe_u32 v90, v57, 16, 1
	v_bfe_u32 v91, v56, 16, 1
	v_perm_b32 v67, v16, v66, s72
	v_perm_b32 v66, v53, v52, s72
	v_perm_b32 v65, v65, v64, s72
	v_perm_b32 v64, v59, v58, s72
	v_bfe_u32 v16, v69, 16, 1
	v_bfe_u32 v52, v68, 16, 1
	v_bfe_u32 v53, v55, 16, 1
	v_bfe_u32 v58, v54, 16, 1
	v_add3_u32 v54, v54, v58, s73
	v_add3_u32 v53, v55, v53, s73
	v_add3_u32 v52, v68, v52, s73
	v_add3_u32 v16, v69, v16, s73
	v_add3_u32 v55, v56, v91, s73
	v_add3_u32 v56, v57, v90, s73
	v_add3_u32 v57, v70, v89, s73
	v_add3_u32 v58, v71, v88, s73
	v_perm_b32 v71, v58, v57, s72
	v_perm_b32 v70, v56, v55, s72
	v_perm_b32 v69, v16, v52, s72
	v_perm_b32 v68, v53, v54, s72
	v_and_b32_e32 v53, 0xffff0000, v60
	v_lshlrev_b32_e32 v52, 16, v60
	v_and_b32_e32 v55, 0xffff0000, v61
	v_lshlrev_b32_e32 v54, 16, v61
	v_and_b32_e32 v57, 0xffff0000, v62
	v_lshlrev_b32_e32 v56, 16, v62
	v_and_b32_e32 v59, 0xffff0000, v63
	v_lshlrev_b32_e32 v58, 16, v63
	v_pk_mul_f32 v[52:53], v[84:85], v[52:53] op_sel_hi:[0,1]
	v_pk_mul_f32 v[54:55], v[84:85], v[54:55] op_sel_hi:[0,1]
	v_pk_mul_f32 v[56:57], v[84:85], v[56:57] op_sel_hi:[0,1]
	v_pk_mul_f32 v[58:59], v[84:85], v[58:59] op_sel_hi:[0,1]
	v_bfe_u32 v16, v59, 16, 1
	v_bfe_u32 v60, v58, 16, 1
	v_bfe_u32 v61, v57, 16, 1
	v_bfe_u32 v62, v56, 16, 1
	v_bfe_u32 v63, v55, 16, 1
; __device__ __forceinline__ bf16 f2bf(float f) { unsigned u = __float_as_uint(f); return (bf16)((u + 0x7fffu + ((u >> 16) & 1u)) >> 16); }
; __device__ __forceinline__ bool run_unit2(LAS unsigned char* lds, const bf16* y0, const float* aux, unsigned* maskg, int b, int g, int tid_in, int wave, int lane) {
;     ...
;     const f32x4 w4 = *(const f32x4*)(aux + (rowbase + t0 + r) * 16 + 8);
;     f32x4 lo4, hi4;
; #pragma unroll
;     for (int hd = 0; hd < 4; ++hd) {
;         const float wsc = w4[hd] * 0.0625f;
;         lo4[hd] = (w4[hd] >= 0.f) ? 0.f : -INFINITY; hi4[hd] = (w4[hd] >= 0.f) ? INFINITY : 0.f;
; #pragma unroll
;         for (int s = 0; s < 4; ++s) {
;             bf16x8 a = qf[hd][s];
; #pragma unroll
;             for (int j = 0; j < 8; ++j) a[j] = (short)f2bf(__uint_as_float(((unsigned)(unsigned short)a[j]) << 16) * wsc);
;             qf[hd][s] = a;
;         }
;     }
	v_bfe_u32 v72, v54, 16, 1
	v_bfe_u32 v73, v53, 16, 1
	v_bfe_u32 v74, v52, 16, 1
	v_add3_u32 v52, v52, v74, s73
	v_add3_u32 v53, v53, v73, s73
	v_add3_u32 v54, v54, v72, s73
	v_add3_u32 v55, v55, v63, s73
	v_add3_u32 v56, v56, v62, s73
	v_add3_u32 v57, v57, v61, s73
	v_add3_u32 v58, v58, v60, s73
	v_add3_u32 v16, v59, v16, s73
	v_perm_b32 v75, v16, v58, s72
	v_perm_b32 v74, v57, v56, s72
	v_perm_b32 v73, v55, v54, s72
	v_perm_b32 v72, v53, v52, s72
	v_and_b32_e32 v53, 0xffff0000, v76
	v_lshlrev_b32_e32 v52, 16, v76
	v_and_b32_e32 v55, 0xffff0000, v77
	v_lshlrev_b32_e32 v54, 16, v77
	v_and_b32_e32 v57, 0xffff0000, v78
	v_lshlrev_b32_e32 v56, 16, v78
	v_and_b32_e32 v59, 0xffff0000, v79
	v_lshlrev_b32_e32 v58, 16, v79
	v_pk_mul_f32 v[52:53], v[84:85], v[52:53] op_sel_hi:[0,1]
	v_pk_mul_f32 v[54:55], v[84:85], v[54:55] op_sel_hi:[0,1]
	v_pk_mul_f32 v[56:57], v[84:85], v[56:57] op_sel_hi:[0,1]
	v_pk_mul_f32 v[58:59], v[84:85], v[58:59] op_sel_hi:[0,1]
	v_bfe_u32 v16, v59, 16, 1
	v_bfe_u32 v60, v58, 16, 1
	v_bfe_u32 v61, v57, 16, 1
	v_bfe_u32 v62, v56, 16, 1
	v_bfe_u32 v63, v55, 16, 1
	v_bfe_u32 v76, v54, 16, 1
	v_bfe_u32 v77, v53, 16, 1
	v_bfe_u32 v78, v52, 16, 1
	v_add3_u32 v52, v52, v78, s73
	v_add3_u32 v53, v53, v77, s73
	v_add3_u32 v54, v54, v76, s73
	v_add3_u32 v55, v55, v63, s73
	v_add3_u32 v56, v56, v62, s73
	v_add3_u32 v57, v57, v61, s73
	v_add3_u32 v58, v58, v60, s73
	v_add3_u32 v16, v59, v16, s73
	v_perm_b32 v79, v16, v58, s72
	v_perm_b32 v78, v57, v56, s72
	v_perm_b32 v77, v55, v54, s72
	v_perm_b32 v76, v53, v52, s72
	v_mul_f32_e32 v16, 0x3d800000, v17
	v_and_b32_e32 v53, 0xffff0000, v80
	v_lshlrev_b32_e32 v52, 16, v80
	v_and_b32_e32 v55, 0xffff0000, v81
	v_lshlrev_b32_e32 v54, 16, v81
	v_and_b32_e32 v57, 0xffff0000, v82
	v_lshlrev_b32_e32 v56, 16, v82
	v_pk_mul_f32 v[52:53], v[16:17], v[52:53] op_sel_hi:[0,1]
	v_pk_mul_f32 v[54:55], v[16:17], v[54:55] op_sel_hi:[0,1]
	v_pk_mul_f32 v[56:57], v[16:17], v[56:57] op_sel_hi:[0,1]
	v_and_b32_e32 v59, 0xffff0000, v83
	v_lshlrev_b32_e32 v58, 16, v83
	v_pk_mul_f32 v[58:59], v[16:17], v[58:59] op_sel_hi:[0,1]
	v_bfe_u32 v61, v57, 16, 1
	v_bfe_u32 v62, v56, 16, 1
	v_bfe_u32 v63, v55, 16, 1
	v_bfe_u32 v80, v54, 16, 1
	v_bfe_u32 v81, v53, 16, 1
	v_bfe_u32 v82, v52, 16, 1
	v_cndmask_b32_e64 v207, v188, 0, vcc
	v_cndmask_b32_e32 v208, 0, v189, vcc
	v_cmp_le_f32_e32 vcc, 0, v17
	v_bfe_u32 v17, v59, 16, 1
	v_add3_u32 v52, v52, v82, s73
	v_add3_u32 v53, v53, v81, s73
	v_add3_u32 v54, v54, v80, s73
	v_add3_u32 v55, v55, v63, s73
	v_add3_u32 v56, v56, v62, s73
	v_add3_u32 v57, v57, v61, s73
	v_bfe_u32 v60, v58, 16, 1
	v_add3_u32 v17, v59, v17, s73
	v_perm_b32 v82, v57, v56, s72
	v_perm_b32 v81, v55, v54, s72
	v_perm_b32 v80, v53, v52, s72
	v_and_b32_e32 v53, 0xffff0000, v44
	v_lshlrev_b32_e32 v52, 16, v44
	v_and_b32_e32 v55, 0xffff0000, v45
	v_lshlrev_b32_e32 v54, 16, v45
	v_and_b32_e32 v57, 0xffff0000, v47
	v_lshlrev_b32_e32 v56, 16, v47
	v_add3_u32 v58, v58, v60, s73
	v_pk_mul_f32 v[52:53], v[16:17], v[52:53] op_sel_hi:[0,1]
	v_pk_mul_f32 v[44:45], v[16:17], v[54:55] op_sel_hi:[0,1]
	v_and_b32_e32 v55, 0xffff0000, v46
	v_lshlrev_b32_e32 v54, 16, v46
	v_pk_mul_f32 v[46:47], v[16:17], v[56:57] op_sel_hi:[0,1]
	v_perm_b32 v83, v17, v58, s72
	v_pk_mul_f32 v[54:55], v[16:17], v[54:55] op_sel_hi:[0,1]
	v_bfe_u32 v17, v47, 16, 1
	v_bfe_u32 v56, v46, 16, 1
	v_bfe_u32 v61, v53, 16, 1
	v_bfe_u32 v62, v52, 16, 1
	v_bfe_u32 v59, v45, 16, 1
	v_bfe_u32 v60, v44, 16, 1
	v_add3_u32 v52, v52, v62, s73
	v_add3_u32 v53, v53, v61, s73
	v_add3_u32 v46, v46, v56, s73
	v_add3_u32 v17, v47, v17, s73
	v_add3_u32 v44, v44, v60, s73
	v_add3_u32 v45, v45, v59, s73
	v_perm_b32 v87, v17, v46, s72
	v_perm_b32 v84, v53, v52, s72
	v_and_b32_e32 v47, 0xffff0000, v41
	v_lshlrev_b32_e32 v46, 16, v41
	v_and_b32_e32 v53, 0xffff0000, v43
	v_lshlrev_b32_e32 v52, 16, v43
	v_bfe_u32 v57, v55, 16, 1
	v_bfe_u32 v58, v54, 16, 1
	v_perm_b32 v85, v45, v44, s72
	v_and_b32_e32 v45, 0xffff0000, v40
	v_lshlrev_b32_e32 v44, 16, v40
	v_pk_mul_f32 v[40:41], v[16:17], v[46:47] op_sel_hi:[0,1]
	v_and_b32_e32 v47, 0xffff0000, v42
	v_lshlrev_b32_e32 v46, 16, v42
	v_pk_mul_f32 v[42:43], v[16:17], v[52:53] op_sel_hi:[0,1]
	v_add3_u32 v54, v54, v58, s73
	v_add3_u32 v55, v55, v57, s73
	v_pk_mul_f32 v[44:45], v[16:17], v[44:45] op_sel_hi:[0,1]
	v_pk_mul_f32 v[46:47], v[16:17], v[46:47] op_sel_hi:[0,1]
	v_bfe_u32 v17, v43, 16, 1
	v_bfe_u32 v52, v42, 16, 1
	v_perm_b32 v86, v55, v54, s72
	v_bfe_u32 v55, v41, 16, 1
	v_bfe_u32 v56, v40, 16, 1
	v_bfe_u32 v57, v45, 16, 1
	v_bfe_u32 v58, v44, 16, 1
	v_add3_u32 v42, v42, v52, s73
	v_add3_u32 v17, v43, v17, s73
	v_add3_u32 v44, v44, v58, s73
	v_add3_u32 v45, v45, v57, s73
	v_add3_u32 v40, v40, v56, s73
	v_add3_u32 v41, v41, v55, s73
	v_perm_b32 v91, v17, v42, s72
	v_and_b32_e32 v43, 0xffff0000, v37
	v_lshlrev_b32_e32 v42, 16, v37
	v_perm_b32 v89, v41, v40, s72
	v_perm_b32 v88, v45, v44, s72
	v_and_b32_e32 v41, 0xffff0000, v36
	v_lshlrev_b32_e32 v40, 16, v36
	v_pk_mul_f32 v[36:37], v[16:17], v[42:43] op_sel_hi:[0,1]
	v_and_b32_e32 v43, 0xffff0000, v38
	v_lshlrev_b32_e32 v42, 16, v38
	v_and_b32_e32 v45, 0xffff0000, v39
	v_lshlrev_b32_e32 v44, 16, v39
	v_bfe_u32 v53, v47, 16, 1
	v_bfe_u32 v54, v46, 16, 1
	v_pk_mul_f32 v[40:41], v[16:17], v[40:41] op_sel_hi:[0,1]
	v_pk_mul_f32 v[42:43], v[16:17], v[42:43] op_sel_hi:[0,1]
	v_pk_mul_f32 v[16:17], v[16:17], v[44:45] op_sel_hi:[0,1]
	v_add3_u32 v46, v46, v54, s73
	v_add3_u32 v47, v47, v53, s73
	v_bfe_u32 v38, v17, 16, 1
	v_bfe_u32 v39, v16, 16, 1
	v_perm_b32 v90, v47, v46, s72
	v_bfe_u32 v46, v37, 16, 1
	v_bfe_u32 v47, v36, 16, 1
	v_bfe_u32 v52, v41, 16, 1
	v_bfe_u32 v53, v40, 16, 1
; __device__ __forceinline__ bf16 f2bf(float f) { unsigned u = __float_as_uint(f); return (bf16)((u + 0x7fffu + ((u >> 16) & 1u)) >> 16); }
; __device__ __forceinline__ bool run_unit2(LAS unsigned char* lds, const bf16* y0, const float* aux, unsigned* maskg, int b, int g, int tid_in, int wave, int lane) {
;     ...
;     for (int hd = 0; hd < 4; ++hd) {
;         const float wsc = w4[hd] * 0.0625f;
;         lo4[hd] = (w4[hd] >= 0.f) ? 0.f : -INFINITY; hi4[hd] = (w4[hd] >= 0.f) ? INFINITY : 0.f;
; #pragma unroll
;         for (int s = 0; s < 4; ++s) {
;             bf16x8 a = qf[hd][s];
; #pragma unroll
;             for (int j = 0; j < 8; ++j) a[j] = (short)f2bf(__uint_as_float(((unsigned)(unsigned short)a[j]) << 16) * wsc);
;             qf[hd][s] = a;
;         }
;     }
	v_add3_u32 v16, v16, v39, s73
	v_add3_u32 v17, v17, v38, s73
	v_bfe_u32 v44, v43, 16, 1
	v_bfe_u32 v45, v42, 16, 1
	v_add3_u32 v40, v40, v53, s73
	v_add3_u32 v41, v41, v52, s73
	v_add3_u32 v36, v36, v47, s73
	v_add3_u32 v37, v37, v46, s73
	v_perm_b32 v95, v17, v16, s72
	v_mul_f32_e32 v16, 0x3d800000, v18
	v_and_b32_e32 v39, 0xffff0000, v33
	v_lshlrev_b32_e32 v38, 16, v33
	v_add3_u32 v42, v42, v45, s73
	v_add3_u32 v43, v43, v44, s73
	v_perm_b32 v93, v37, v36, s72
	v_perm_b32 v92, v41, v40, s72
	v_and_b32_e32 v37, 0xffff0000, v32
	v_lshlrev_b32_e32 v36, 16, v32
	v_pk_mul_f32 v[32:33], v[16:17], v[38:39] op_sel_hi:[0,1]
	v_and_b32_e32 v41, 0xffff0000, v35
	v_lshlrev_b32_e32 v40, 16, v35
	v_perm_b32 v94, v43, v42, s72
	v_pk_mul_f32 v[36:37], v[16:17], v[36:37] op_sel_hi:[0,1]
	v_and_b32_e32 v39, 0xffff0000, v34
	v_lshlrev_b32_e32 v38, 16, v34
	v_pk_mul_f32 v[34:35], v[16:17], v[40:41] op_sel_hi:[0,1]
	v_bfe_u32 v42, v33, 16, 1
	v_bfe_u32 v43, v32, 16, 1
	v_cndmask_b32_e64 v209, v188, 0, vcc
	v_cndmask_b32_e32 v210, 0, v189, vcc
	v_cmp_le_f32_e32 vcc, 0, v18
	v_pk_mul_f32 v[38:39], v[16:17], v[38:39] op_sel_hi:[0,1]
	v_bfe_u32 v17, v35, 16, 1
	v_bfe_u32 v18, v34, 16, 1
	v_bfe_u32 v44, v37, 16, 1
	v_bfe_u32 v45, v36, 16, 1
	v_add3_u32 v32, v32, v43, s73
	v_add3_u32 v33, v33, v42, s73
	v_bfe_u32 v40, v39, 16, 1
	v_bfe_u32 v41, v38, 16, 1
	v_add3_u32 v36, v36, v45, s73
	v_add3_u32 v37, v37, v44, s73
	v_add3_u32 v18, v34, v18, s73
	v_add3_u32 v17, v35, v17, s73
	v_perm_b32 v97, v33, v32, s72
	v_and_b32_e32 v33, 0xffff0000, v28
	v_lshlrev_b32_e32 v32, 16, v28
	v_and_b32_e32 v35, 0xffff0000, v29
	v_lshlrev_b32_e32 v34, 16, v29
	v_add3_u32 v38, v38, v41, s73
	v_add3_u32 v39, v39, v40, s73
	v_perm_b32 v96, v37, v36, s72
	v_pk_mul_f32 v[32:33], v[16:17], v[32:33] op_sel_hi:[0,1]
	v_pk_mul_f32 v[28:29], v[16:17], v[34:35] op_sel_hi:[0,1]
	v_and_b32_e32 v37, 0xffff0000, v31
	v_lshlrev_b32_e32 v36, 16, v31
	v_perm_b32 v98, v39, v38, s72
	v_and_b32_e32 v35, 0xffff0000, v30
	v_lshlrev_b32_e32 v34, 16, v30
	v_pk_mul_f32 v[30:31], v[16:17], v[36:37] op_sel_hi:[0,1]
	v_bfe_u32 v38, v29, 16, 1
	v_bfe_u32 v39, v28, 16, 1
	v_bfe_u32 v40, v33, 16, 1
	v_bfe_u32 v41, v32, 16, 1
	v_perm_b32 v99, v17, v18, s72
	v_pk_mul_f32 v[34:35], v[16:17], v[34:35] op_sel_hi:[0,1]
	v_bfe_u32 v17, v31, 16, 1
	v_bfe_u32 v18, v30, 16, 1
	v_add3_u32 v32, v32, v41, s73
	v_add3_u32 v33, v33, v40, s73
	v_add3_u32 v28, v28, v39, s73
	v_add3_u32 v29, v29, v38, s73
	v_bfe_u32 v36, v35, 16, 1
	v_bfe_u32 v37, v34, 16, 1
	v_add3_u32 v18, v30, v18, s73
	v_add3_u32 v17, v31, v17, s73
	v_perm_b32 v101, v29, v28, s72
	v_perm_b32 v100, v33, v32, s72
	v_and_b32_e32 v29, 0xffff0000, v24
	v_lshlrev_b32_e32 v28, 16, v24
	v_and_b32_e32 v31, 0xffff0000, v25
	v_lshlrev_b32_e32 v30, 16, v25
	v_and_b32_e32 v33, 0xffff0000, v27
	v_lshlrev_b32_e32 v32, 16, v27
	v_add3_u32 v34, v34, v37, s73
	v_add3_u32 v35, v35, v36, s73
	v_pk_mul_f32 v[28:29], v[16:17], v[28:29] op_sel_hi:[0,1]
	v_pk_mul_f32 v[24:25], v[16:17], v[30:31] op_sel_hi:[0,1]
	v_and_b32_e32 v31, 0xffff0000, v26
	v_lshlrev_b32_e32 v30, 16, v26
	v_pk_mul_f32 v[26:27], v[16:17], v[32:33] op_sel_hi:[0,1]
	v_perm_b32 v103, v17, v18, s72
	v_perm_b32 v102, v35, v34, s72
	v_pk_mul_f32 v[30:31], v[16:17], v[30:31] op_sel_hi:[0,1]
	v_bfe_u32 v17, v27, 16, 1
	v_bfe_u32 v18, v26, 16, 1
	v_bfe_u32 v34, v25, 16, 1
	v_bfe_u32 v35, v24, 16, 1
	v_bfe_u32 v36, v29, 16, 1
	v_bfe_u32 v37, v28, 16, 1
	v_add3_u32 v28, v28, v37, s73
	v_add3_u32 v29, v29, v36, s73
	v_add3_u32 v24, v24, v35, s73
	v_add3_u32 v25, v25, v34, s73
	v_add3_u32 v18, v26, v18, s73
	v_add3_u32 v17, v27, v17, s73
	v_and_b32_e32 v27, 0xffff0000, v21
	v_lshlrev_b32_e32 v26, 16, v21
	v_bfe_u32 v32, v31, 16, 1
	v_bfe_u32 v33, v30, 16, 1
	v_perm_b32 v105, v25, v24, s72
	v_perm_b32 v104, v29, v28, s72
	v_and_b32_e32 v25, 0xffff0000, v20
	v_lshlrev_b32_e32 v24, 16, v20
	v_pk_mul_f32 v[20:21], v[16:17], v[26:27] op_sel_hi:[0,1]
	v_and_b32_e32 v27, 0xffff0000, v22
	v_lshlrev_b32_e32 v26, 16, v22
	v_and_b32_e32 v29, 0xffff0000, v23
	v_lshlrev_b32_e32 v28, 16, v23
	v_add3_u32 v30, v30, v33, s73
	v_add3_u32 v31, v31, v32, s73
	v_perm_b32 v107, v17, v18, s72
	v_pk_mul_f32 v[24:25], v[16:17], v[24:25] op_sel_hi:[0,1]
	v_pk_mul_f32 v[26:27], v[16:17], v[26:27] op_sel_hi:[0,1]
	v_pk_mul_f32 v[16:17], v[16:17], v[28:29] op_sel_hi:[0,1]
	v_perm_b32 v106, v31, v30, s72
	v_bfe_u32 v18, v17, 16, 1
	v_bfe_u32 v22, v16, 16, 1
	v_bfe_u32 v23, v27, 16, 1
	v_bfe_u32 v28, v26, 16, 1
	v_bfe_u32 v29, v21, 16, 1
	v_bfe_u32 v30, v20, 16, 1
	v_add3_u32 v20, v20, v30, s73
	v_add3_u32 v21, v21, v29, s73
	v_add3_u32 v26, v26, v28, s73
	v_add3_u32 v23, v27, v23, s73
	v_add3_u32 v16, v16, v22, s73
	v_add3_u32 v17, v17, v18, s73
	v_cndmask_b32_e64 v212, v188, 0, vcc
	v_cndmask_b32_e32 v213, 0, v189, vcc
	v_bfe_u32 v31, v25, 16, 1
	v_bfe_u32 v32, v24, 16, 1
	v_perm_b32 v111, v17, v16, s72
	v_perm_b32 v110, v23, v26, s72
	v_perm_b32 v109, v21, v20, s72
; __device__ __forceinline__ bf16 f2bf(float f) { unsigned u = __float_as_uint(f); return (bf16)((u + 0x7fffu + ((u >> 16) & 1u)) >> 16); }
; #define DSA2_LOADK(dst, kt_) do { _Pragma("unroll") for (int s = 0; s < 4; ++s) dst[s] = *(const bf16x8*)(kp + (size_t)(32 * (kt_)) * Y0P + 16 * s); } while (0)
; template <int STAGE>
; __device__ __forceinline__ void pass2(LAS unsigned char* lds, const bf16* kbase, int g, int t0, const bf16x8 (&qf)[4][4], const f32x4 lo4, const f32x4 hi4, int wave, int r, int h2) {
;     ...
;     int kt = wave;
;     if (kt <= g) DSA2_LOADK(kf, kt);
;     for (;;) {
;         if (kt > g) break;
;         if (kt + 8 <= g) DSA2_LOADK(kn, kt + 8);
; __device__ __forceinline__ bool run_unit2(LAS unsigned char* lds, const bf16* y0, const float* aux, unsigned* maskg, int b, int g, int tid_in, int wave, int lane) {
;     ...
;     for (int hd = 0; hd < 4; ++hd) {
;         const float wsc = w4[hd] * 0.0625f;
;         lo4[hd] = (w4[hd] >= 0.f) ? 0.f : -INFINITY; hi4[hd] = (w4[hd] >= 0.f) ? INFINITY : 0.f;
; #pragma unroll
;         for (int s = 0; s < 4; ++s) {
;             bf16x8 a = qf[hd][s];
; #pragma unroll
;             for (int j = 0; j < 8; ++j) a[j] = (short)f2bf(__uint_as_float(((unsigned)(unsigned short)a[j]) << 16) * wsc);
;             qf[hd][s] = a;
;         }
	v_mul_f32_e32 v16, 0x3d800000, v19
	v_cmp_le_f32_e32 vcc, 0, v19
	v_and_b32_e32 v19, 0xffff0000, v12
	v_lshlrev_b32_e32 v18, 16, v12
	v_and_b32_e32 v21, 0xffff0000, v13
	v_lshlrev_b32_e32 v20, 16, v13
	v_and_b32_e32 v23, 0xffff0000, v15
	v_lshlrev_b32_e32 v22, 16, v15
	v_add3_u32 v24, v24, v32, s73
	v_add3_u32 v25, v25, v31, s73
	v_pk_mul_f32 v[18:19], v[16:17], v[18:19] op_sel_hi:[0,1]
	v_pk_mul_f32 v[12:13], v[16:17], v[20:21] op_sel_hi:[0,1]
	v_and_b32_e32 v21, 0xffff0000, v14
	v_lshlrev_b32_e32 v20, 16, v14
	v_pk_mul_f32 v[14:15], v[16:17], v[22:23] op_sel_hi:[0,1]
	v_perm_b32 v108, v25, v24, s72
	v_pk_mul_f32 v[20:21], v[16:17], v[20:21] op_sel_hi:[0,1]
	v_bfe_u32 v17, v15, 16, 1
	v_bfe_u32 v22, v14, 16, 1
	v_bfe_u32 v25, v13, 16, 1
	v_bfe_u32 v26, v12, 16, 1
	v_bfe_u32 v27, v19, 16, 1
	v_bfe_u32 v28, v18, 16, 1
	v_add3_u32 v18, v18, v28, s73
	v_add3_u32 v19, v19, v27, s73
	v_add3_u32 v12, v12, v26, s73
	v_add3_u32 v13, v13, v25, s73
	v_add3_u32 v14, v14, v22, s73
	v_add3_u32 v15, v15, v17, s73
	v_perm_b32 v115, v15, v14, s72
	v_perm_b32 v113, v13, v12, s72
	v_perm_b32 v112, v19, v18, s72
	v_and_b32_e32 v13, 0xffff0000, v8
	v_lshlrev_b32_e32 v12, 16, v8
	v_and_b32_e32 v15, 0xffff0000, v9
	v_lshlrev_b32_e32 v14, 16, v9
	v_and_b32_e32 v19, 0xffff0000, v11
	v_lshlrev_b32_e32 v18, 16, v11
	v_bfe_u32 v23, v21, 16, 1
	v_bfe_u32 v24, v20, 16, 1
	v_pk_mul_f32 v[12:13], v[16:17], v[12:13] op_sel_hi:[0,1]
	v_pk_mul_f32 v[8:9], v[16:17], v[14:15] op_sel_hi:[0,1]
	v_and_b32_e32 v15, 0xffff0000, v10
	v_lshlrev_b32_e32 v14, 16, v10
	v_pk_mul_f32 v[10:11], v[16:17], v[18:19] op_sel_hi:[0,1]
	v_add3_u32 v20, v20, v24, s73
	v_add3_u32 v21, v21, v23, s73
	v_pk_mul_f32 v[14:15], v[16:17], v[14:15] op_sel_hi:[0,1]
	v_bfe_u32 v17, v11, 16, 1
	v_bfe_u32 v18, v10, 16, 1
	v_bfe_u32 v23, v13, 16, 1
	v_bfe_u32 v24, v12, 16, 1
	v_perm_b32 v114, v21, v20, s72
	v_bfe_u32 v21, v9, 16, 1
	v_bfe_u32 v22, v8, 16, 1
	v_add3_u32 v12, v12, v24, s73
	v_add3_u32 v13, v13, v23, s73
	v_add3_u32 v10, v10, v18, s73
	v_add3_u32 v11, v11, v17, s73
	v_add3_u32 v8, v8, v22, s73
	v_add3_u32 v9, v9, v21, s73
	v_perm_b32 v119, v11, v10, s72
	v_perm_b32 v116, v13, v12, s72
	v_and_b32_e32 v11, 0xffff0000, v5
	v_lshlrev_b32_e32 v10, 16, v5
	v_and_b32_e32 v13, 0xffff0000, v7
	v_lshlrev_b32_e32 v12, 16, v7
	v_perm_b32 v117, v9, v8, s72
	v_and_b32_e32 v9, 0xffff0000, v4
	v_lshlrev_b32_e32 v8, 16, v4
	v_pk_mul_f32 v[4:5], v[16:17], v[10:11] op_sel_hi:[0,1]
	v_and_b32_e32 v11, 0xffff0000, v6
	v_lshlrev_b32_e32 v10, 16, v6
	v_pk_mul_f32 v[6:7], v[16:17], v[12:13] op_sel_hi:[0,1]
	v_bfe_u32 v19, v15, 16, 1
	v_bfe_u32 v20, v14, 16, 1
	v_pk_mul_f32 v[8:9], v[16:17], v[8:9] op_sel_hi:[0,1]
	v_bfe_u32 v12, v7, 16, 1
	v_bfe_u32 v13, v6, 16, 1
	v_add3_u32 v14, v14, v20, s73
	v_add3_u32 v15, v15, v19, s73
	v_pk_mul_f32 v[10:11], v[16:17], v[10:11] op_sel_hi:[0,1]
	v_bfe_u32 v17, v5, 16, 1
	v_bfe_u32 v18, v4, 16, 1
	v_bfe_u32 v19, v9, 16, 1
	v_bfe_u32 v20, v8, 16, 1
	v_add3_u32 v6, v6, v13, s73
	v_add3_u32 v7, v7, v12, s73
	v_add3_u32 v8, v8, v20, s73
	v_add3_u32 v9, v9, v19, s73
	v_add3_u32 v4, v4, v18, s73
	v_add3_u32 v5, v5, v17, s73
	v_perm_b32 v123, v7, v6, s72
	v_and_b32_e32 v7, 0xffff0000, v1
	v_lshlrev_b32_e32 v6, 16, v1
	v_perm_b32 v118, v15, v14, s72
	v_bfe_u32 v14, v11, 16, 1
	v_bfe_u32 v15, v10, 16, 1
	v_perm_b32 v121, v5, v4, s72
	v_perm_b32 v120, v9, v8, s72
	v_and_b32_e32 v5, 0xffff0000, v0
	v_lshlrev_b32_e32 v4, 16, v0
	v_pk_mul_f32 v[0:1], v[16:17], v[6:7] op_sel_hi:[0,1]
	v_and_b32_e32 v7, 0xffff0000, v2
	v_lshlrev_b32_e32 v6, 16, v2
	v_and_b32_e32 v9, 0xffff0000, v3
	v_lshlrev_b32_e32 v8, 16, v3
	v_add3_u32 v10, v10, v15, s73
	v_add3_u32 v11, v11, v14, s73
	v_pk_mul_f32 v[4:5], v[16:17], v[4:5] op_sel_hi:[0,1]
	v_pk_mul_f32 v[6:7], v[16:17], v[6:7] op_sel_hi:[0,1]
	v_pk_mul_f32 v[2:3], v[16:17], v[8:9] op_sel_hi:[0,1]
	v_bfe_u32 v12, v1, 16, 1
	v_bfe_u32 v13, v0, 16, 1
	v_perm_b32 v122, v11, v10, s72
	v_bfe_u32 v8, v3, 16, 1
	v_bfe_u32 v9, v2, 16, 1
	v_bfe_u32 v10, v7, 16, 1
	v_bfe_u32 v11, v6, 16, 1
	v_bfe_u32 v14, v5, 16, 1
	v_bfe_u32 v15, v4, 16, 1
	v_add3_u32 v0, v0, v13, s73
	v_add3_u32 v1, v1, v12, s73
	v_add3_u32 v4, v4, v15, s73
	v_add3_u32 v5, v5, v14, s73
	v_add3_u32 v6, v6, v11, s73
	v_add3_u32 v7, v7, v10, s73
	v_add3_u32 v2, v2, v9, s73
	v_add3_u32 v3, v3, v8, s73
	v_perm_b32 v125, v1, v0, s72
	v_lshl_add_u64 v[0:1], s[80:81], 0, v[176:177]
	v_cndmask_b32_e64 v214, v188, 0, vcc
	v_cndmask_b32_e32 v215, 0, v189, vcc
	v_perm_b32 v127, v3, v2, s72
	v_perm_b32 v126, v7, v6, s72
	v_perm_b32 v124, v5, v4, s72
	v_lshl_add_u64 v[178:179], v[0:1], 0, v[50:51]
	s_cbranch_scc1 .LBB0_804
	v_lshl_add_u64 v[0:1], v[48:49], 1, s[78:79]
	v_lshl_add_u64 v[0:1], v[0:1], 0, v[176:177]
	v_mad_u32_u24 v204, v218, s26, 0
	v_lshl_add_u64 v[180:181], s[34:35], 0, v[0:1]
	s_sub_i32 s0, 0, s64
	s_mov_b32 s1, s30
	s_mov_b32 s6, s92
	v_readlane_b32 s98, v254, 24
	s_cmp_lt_u32 s98, 4
	s_cbranch_scc1 .Lp4stag0
	s_sleep 14

; #define LAS __attribute__((address_space(3)))
; __device__ __forceinline__ int bin2(float sv, int zi) {
;     const unsigned u = __float_as_uint(sv);
;     int c = (int)((u >> 20) & 0x7FFu) - 832;
;     c = c < 0 ? 0 : (c > 207 ? 207 : c);
;     int b = (u >> 31) ? (207 - c) : (272 + c);
;     if (sv == 0.0f) b = 208 + zi;
;     return b;
; }
; template <int STAGE>
; __device__ __forceinline__ void pass2(LAS unsigned char* lds, const bf16* kbase, int g, int t0, const bf16x8 (&qf)[4][4], const f32x4 lo4, const f32x4 hi4, int wave, int r, int h2) {
;     LAS unsigned* hist = (LAS unsigned*)(lds + OFF2_HIST);
;     LAS unsigned long long* cand = (LAS unsigned long long*)(lds + OFF2_CAND);
;     LAS unsigned* gtm = (LAS unsigned*)(lds + OFF2_GT);
;     LAS unsigned* cntp = (LAS unsigned*)(lds + OFF2_CNT);
;     const int tq = t0 + r;
;     const int tb = (STAGE == 1) ? ((const LAS int*)(lds + OFF2_TB))[r] : 0;
;     bf16x8 kf[4], kn[4];
;     const bf16* kp = kbase + (size_t)r * Y0P + 8 * h2;
.LBB0_822:
	s_or_b64 exec, exec, s[4:5]
	s_andn2_b64 vcc, exec, s[82:83]
	s_waitcnt lgkmcnt(0)
	s_barrier
	s_cbranch_vccnz .LBB0_880
	v_lshlrev_b32_e32 v0, 2, v218
	v_add_u32_e32 v1, 0, v0
	v_add_u32_e32 v1, 0x18100, v1
	ds_read_b32 v222, v1
	s_add_i32 s0, 0, 0x18200
	v_lshlrev_b32_e32 v1, 9, v219
	v_lshlrev_b32_e32 v2, 4, v218
	v_add_u32_e32 v224, s0, v0
	v_mov_b32_e32 v0, s27
	v_add3_u32 v223, s65, v1, v2
	v_lshlrev_b32_e32 v219, 2, v219
	v_lshl_add_u32 v225, v218, 11, 0
	v_cmp_gt_u32_e64 s[84:85], 32, v217
	v_mad_u32_u24 v217, v218, s24, v0
	v_readlane_b32 s0, v254, 24
	s_waitcnt lgkmcnt(0)
	v_sub_u32_e32 v0, 0xcf, v222
	v_add_u32_e32 v0, 0x340, v0
	v_lshlrev_b32_e32 v0, 20, v0
	v_add_u32_e32 v0, 0x7fffffff, v0
	v_add_u32_e32 v1, 0x100000, v0
	v_add_u32_e32 v2, 0x230, v222
	v_lshlrev_b32_e32 v2, 20, v2
	v_add_u32_e32 v3, 0x100000, v2
	v_mov_b32_e32 v4, 0xff800000
	v_bfrev_b32_e32 v5, 1
	v_mov_b32_e32 v6, 1
	v_mov_b32_e32 v7, 0x7fc00000
	v_mov_b32_e32 v8, 0x7fffffff
	v_cmp_gt_i32_e32 vcc, 0, v222
	s_nop 1
	v_cndmask_b32_e32 v252, v0, v4, vcc
	v_cmp_eq_u32_e32 vcc, 0xcf, v222
	s_nop 1
	v_cndmask_b32_e32 v252, v252, v5, vcc
	v_cmp_lt_i32_e32 vcc, 0xcf, v222
	s_nop 1
	v_cndmask_b32_e32 v252, v252, v6, vcc
	v_cmp_lt_i32_e32 vcc, 0x10f, v222
	s_nop 1
	v_cndmask_b32_e32 v252, v252, v3, vcc
	v_cmp_eq_u32_e32 vcc, 0x1df, v222
	s_nop 1
	v_cndmask_b32_e32 v252, v252, v7, vcc
	v_cmp_gt_i32_e32 vcc, 1, v222
	s_nop 1
	v_cndmask_b32_e32 v253, v1, v4, vcc
	v_cmp_lt_i32_e32 vcc, 0xcf, v222
	s_nop 1
	v_cndmask_b32_e32 v253, v253, v6, vcc
	v_cmp_lt_i32_e32 vcc, 0x110, v222
	s_nop 1
	v_cndmask_b32_e32 v253, v253, v2, vcc
	v_cmp_lt_i32_e32 vcc, 0xcf, v222
	s_nop 1
	v_cndmask_b32_e32 v232, v8, v222, vcc
	v_cmp_lt_i32_e32 vcc, 0x10f, v222
	s_nop 1
	v_cndmask_b32_e32 v232, v232, v8, vcc
	s_cmp_lt_u32 s0, 4
	s_cbranch_scc1 .Lp4stag1
	s_sleep 14
